# phase-0 weight preparation: tile index permuted so consecutive waves read neighbouring column pieces of the f32 weights
# speedup vs baseline: 1.0014x; 1.0014x over previous
.LBB0_34:
	s_xor_b64 s[4:5], s[4:5], -1
	v_writelane_b32 v255, s4, 36
	s_andn2_b64 vcc, exec, s[6:7]
	s_nop 0
	v_writelane_b32 v255, s5, 37
	v_writelane_b32 v255, s74, 38
	s_cbranch_vccnz .LBB0_199
	v_mov_b32_e32 v50, v0
	s_mov_b64 s[20:21], 0
	v_readfirstlane_b32 s4, v50
	s_ashr_i32 s46, s4, 6
	v_readlane_b32 s4, v252, 2
	v_readlane_b32 s6, v252, 4
	v_readlane_b32 s7, v252, 5
	s_add_u32 s14, s6, s20
	s_addc_u32 s15, s7, s21
	s_add_u32 s10, s86, s20
	v_readlane_b32 s4, v254, 44
	s_addc_u32 s11, s87, s21
	s_add_i32 s18, s46, s4
	v_and_b32_e32 v51, 63, v50
	s_cmpk_gt_i32 s18, 0x2a7f
	s_mov_b32 s51, s57
	v_readlane_b32 s5, v252, 3
	s_cbranch_scc1 .LBB0_120
	s_load_dwordx2 s[4:5], s[10:11], 0x20
	s_mov_b64 s[8:9], s[50:51]
	s_mul_i32 s6, s8, 0x1ab8000
	v_lshlrev_b32_e32 v2, 3, v51
	v_lshrrev_b32_e32 v20, 3, v51
	s_waitcnt lgkmcnt(0)
	s_add_u32 s22, s4, s6
	s_addc_u32 s23, s5, 0
	s_lshl_b32 s4, s46, 14
	s_lshl_b64 s[6:7], s[50:51], 24
	s_add_i32 s4, s4, 0
	s_add_u32 s42, s14, 0x3980000
	s_addc_u32 s43, s15, 0
	s_add_u32 s44, s14, 0x3180000
	v_writelane_b32 v255, s6, 39
	s_addc_u32 s45, s15, 0
	s_lshl_b32 s48, s8, 10
	v_writelane_b32 v255, s7, 40
	s_add_u32 s6, s10, 0xd0
	s_addc_u32 s7, s11, 0
	v_writelane_b32 v255, s6, 41
	s_lshl_b64 s[52:53], s[50:51], 22
	v_and_b32_e32 v4, 56, v2
	v_writelane_b32 v255, s7, 42
	s_add_u32 s6, s10, 0xc8
	s_addc_u32 s7, s11, 0
	v_writelane_b32 v255, s6, 43
	v_mul_u32_u24_e32 v2, 0x84, v4
	v_lshlrev_b32_e32 v6, 2, v20
	v_writelane_b32 v255, s7, 44
	s_add_u32 s6, s10, 0xc0
	s_addc_u32 s7, s11, 0
	v_writelane_b32 v255, s6, 45
	v_and_b32_e32 v5, 31, v50
	v_add3_u32 v21, s4, v2, v6
	v_writelane_b32 v255, s7, 46
	s_add_u32 s6, s10, 0xd8
	s_addc_u32 s7, s11, 0
	s_add_u32 s70, s10, 0xa8
	s_addc_u32 s71, s11, 0
	s_add_u32 s72, s14, 0x2b80000
	v_writelane_b32 v255, s6, 47
	s_addc_u32 s73, s15, 0
	v_lshlrev_b32_e32 v2, 1, v4
	v_writelane_b32 v255, s7, 48
	s_add_u32 s6, s14, 0x2980000
	s_addc_u32 s7, s15, 0
	s_add_u32 s60, s14, 0x2780000
	s_addc_u32 s61, s15, 0
	v_lshl_add_u32 v19, v5, 2, s4
	v_lshl_add_u64 v[10:11], s[14:15], 0, v[2:3]
	s_mov_b64 s[4:5], 0x1780000
	v_lshlrev_b32_e32 v2, 4, v50
	v_writelane_b32 v255, s6, 49
	s_add_u32 s19, s14, 0x1f80000
	v_lshl_add_u64 v[6:7], v[10:11], 0, s[4:5]
	s_mov_b64 s[4:5], 0x1680000
	v_and_b32_e32 v2, 16, v2
	v_bfe_u32 v12, v50, 1, 4
	v_writelane_b32 v255, s7, 50
	v_lshrrev_b32_e32 v18, 5, v51
	s_addc_u32 s47, s15, 0
	v_lshl_add_u64 v[8:9], v[10:11], 0, s[4:5]
	v_or3_b32 v27, v12, v2, s67
	s_lshl_b32 s56, s8, 7
	s_lshl_b32 s4, s8, 8
	s_mov_b32 s5, s57
	s_mov_b64 s[6:7], 0x1100000
	v_lshlrev_b32_e32 v2, 10, v20
	s_mov_b32 s49, s57
	v_or_b32_e32 v22, 8, v20
	v_or_b32_e32 v23, 16, v20
	v_or_b32_e32 v24, 24, v20
	v_bfe_u32 v25, v50, 4, 1
	v_and_b32_e32 v26, 15, v50
	s_lshl_b64 s[94:95], s[50:51], 18
	v_or_b32_e32 v28, 0xffffff00, v18
	v_lshl_add_u64 v[10:11], v[10:11], 0, s[6:7]
	v_lshl_add_u64 v[12:13], v[8:9], 0, v[2:3]
	s_lshl_b64 s[12:13], s[56:57], 2
	s_lshl_b64 s[64:65], s[4:5], 2
	s_mov_b32 s32, s18
	s_branch .LBB0_38
.LBB0_37:
	s_add_i32 s32, s32, s90
	s_cmpk_gt_i32 s32, 0x2a7f
	s_cbranch_scc1 .LBB0_120
.LBB0_38:
	s_cmpk_lt_u32 s32, 0x580
	s_cbranch_scc0 .Lwp_pow2
	s_mul_i32 s4, s32, 0x2e9
	s_lshr_b32 s4, s4, 16
	s_mul_i32 s5, s4, 0x58
	s_sub_i32 s5, s32, s5
	s_lshl_b32 s5, s5, 4
	s_add_i32 s58, s5, s4
	s_branch .Lwp_done
.Lwp_pow2:
	s_movk_i32 s4, 0x580
	s_mov_b32 s5, 5
	s_mov_b32 s6, 3
	s_cmpk_lt_u32 s32, 0x680
	s_cbranch_scc1 .Lwp_go
	s_movk_i32 s4, 0x680
	s_mov_b32 s5, 7
	s_mov_b32 s6, 4
	s_cmpk_lt_u32 s32, 0xe80
	s_cbranch_scc1 .Lwp_go
	s_movk_i32 s4, 0xe80
	s_mov_b32 s5, 5
	s_mov_b32 s6, 2
	s_cmpk_lt_u32 s32, 0x1080
	s_cbranch_scc1 .Lwp_go
	s_movk_i32 s4, 0x1080
	s_mov_b32 s5, 5
	s_mov_b32 s6, 4
	s_cmpk_lt_u32 s32, 0x1a80
	s_cbranch_scc1 .Lwp_go
	s_movk_i32 s4, 0x1a80
	s_mov_b32 s5, 7
	s_mov_b32 s6, 4
	s_cmpk_lt_u32 s32, 0x2280
	s_cbranch_scc1 .Lwp_go
	s_movk_i32 s4, 0x2280
	s_mov_b32 s5, 5
	s_mov_b32 s6, 6
.Lwp_go:
	s_sub_i32 s7, s32, s4
	s_add_i32 s16, s5, s6
	s_lshr_b32 s17, s7, s16
	s_lshl_b32 s17, s17, s16
	s_sub_i32 s7, s7, s17
	s_add_i32 s4, s4, s17
	s_lshr_b32 s17, s7, s5
	s_lshl_b32 s16, s17, s5
	s_sub_i32 s7, s7, s16
	s_lshl_b32 s7, s7, s6
	s_add_i32 s4, s4, s7
	s_add_i32 s58, s4, s17
